# NA/window loops: counted lgkmcnt wait per P.V MFMA instead of lgkmcnt(0) per group of four
# baseline (speedup 1.0000x reference)
.LBB0_612:
	s_add_i32 s8, s19, 3
	s_cmp_lt_u32 s8, 12
	s_cselect_b64 s[10:11], -1, 0
	s_cmp_eq_u32 s101, 1
	s_cbranch_scc1 .Lna_pvdB
	ds_read_b64_tr_b16 v[238:239], v202 offset:0
	ds_read_b64_tr_b16 v[240:241], v202 offset:0x800
	ds_read_b64_tr_b16 v[242:243], v202 offset:0x1000
	ds_read_b64_tr_b16 v[244:245], v202 offset:0x1800
	ds_read_b64_tr_b16 v[246:247], v202 offset:0x2000
	ds_read_b64_tr_b16 v[248:249], v202 offset:0x2800
	ds_read_b64_tr_b16 v[250:251], v202 offset:0x3000
	ds_read_b64_tr_b16 v[252:253], v202 offset:0x3800
	s_nop 0
	s_waitcnt lgkmcnt(6)
	v_mfma_f32_32x32x16_bf16 v[0:15], v[144:147], v[238:241], v[0:15]
	ds_read_b64_tr_b16 v[238:239], v202 offset:0x200
	ds_read_b64_tr_b16 v[240:241], v202 offset:0xa00
	s_waitcnt lgkmcnt(6)
	v_mfma_f32_32x32x16_bf16 v[0:15], v[234:237], v[242:245], v[0:15]
	ds_read_b64_tr_b16 v[242:243], v202 offset:0x1200
	ds_read_b64_tr_b16 v[244:245], v202 offset:0x1a00
	s_waitcnt lgkmcnt(6)
	v_mfma_f32_32x32x16_bf16 v[0:15], v[226:229], v[246:249], v[0:15]
	ds_read_b64_tr_b16 v[246:247], v202 offset:0x2200
	ds_read_b64_tr_b16 v[248:249], v202 offset:0x2a00
	s_waitcnt lgkmcnt(6)
	v_mfma_f32_32x32x16_bf16 v[0:15], v[230:233], v[250:253], v[0:15]
	ds_read_b64_tr_b16 v[250:251], v202 offset:0x3200
	ds_read_b64_tr_b16 v[252:253], v202 offset:0x3a00
	s_waitcnt lgkmcnt(6)
	v_mfma_f32_32x32x16_bf16 v[48:63], v[144:147], v[238:241], v[48:63]
	ds_read_b64_tr_b16 v[238:239], v202 offset:0x400
	ds_read_b64_tr_b16 v[240:241], v202 offset:0xc00
	s_waitcnt lgkmcnt(6)
	v_mfma_f32_32x32x16_bf16 v[48:63], v[234:237], v[242:245], v[48:63]
	ds_read_b64_tr_b16 v[242:243], v202 offset:0x1400
	ds_read_b64_tr_b16 v[244:245], v202 offset:0x1c00
	s_waitcnt lgkmcnt(6)
	v_mfma_f32_32x32x16_bf16 v[48:63], v[226:229], v[246:249], v[48:63]
	ds_read_b64_tr_b16 v[246:247], v202 offset:0x2400
	ds_read_b64_tr_b16 v[248:249], v202 offset:0x2c00
	s_waitcnt lgkmcnt(6)
	v_mfma_f32_32x32x16_bf16 v[48:63], v[230:233], v[250:253], v[48:63]
	ds_read_b64_tr_b16 v[250:251], v202 offset:0x3400
	ds_read_b64_tr_b16 v[252:253], v202 offset:0x3c00
	s_waitcnt lgkmcnt(6)
	v_mfma_f32_32x32x16_bf16 v[32:47], v[144:147], v[238:241], v[32:47]
	ds_read_b64_tr_b16 v[238:239], v202 offset:0x600
	ds_read_b64_tr_b16 v[240:241], v202 offset:0xe00
	s_waitcnt lgkmcnt(6)
	v_mfma_f32_32x32x16_bf16 v[32:47], v[234:237], v[242:245], v[32:47]
	ds_read_b64_tr_b16 v[242:243], v202 offset:0x1600
	ds_read_b64_tr_b16 v[244:245], v202 offset:0x1e00
	s_waitcnt lgkmcnt(6)
	v_mfma_f32_32x32x16_bf16 v[32:47], v[226:229], v[246:249], v[32:47]
	ds_read_b64_tr_b16 v[246:247], v202 offset:0x2600
	ds_read_b64_tr_b16 v[248:249], v202 offset:0x2e00
	s_waitcnt lgkmcnt(6)
	v_mfma_f32_32x32x16_bf16 v[32:47], v[230:233], v[250:253], v[32:47]
	ds_read_b64_tr_b16 v[250:251], v202 offset:0x3600
	ds_read_b64_tr_b16 v[252:253], v202 offset:0x3e00
	s_waitcnt lgkmcnt(6)
	v_mfma_f32_32x32x16_bf16 v[16:31], v[144:147], v[238:241], v[16:31]
	v_max_f32_e32 v144, v81, v81
	v_max_f32_e32 v145, v80, v80
	v_max_f32_e32 v144, v145, v144
	v_max3_f32 v144, v144, v82, v83
	v_max3_f32 v144, v144, v84, v85
	v_max3_f32 v144, v144, v86, v87
	v_max3_f32 v144, v144, v88, v89
	v_max3_f32 v144, v144, v90, v91
	v_max3_f32 v144, v144, v92, v93
	s_waitcnt lgkmcnt(4)
	v_mfma_f32_32x32x16_bf16 v[16:31], v[234:237], v[242:245], v[16:31]
	v_max3_f32 v144, v144, v94, v95
	v_max3_f32 v144, v144, v64, v65
	v_max3_f32 v144, v144, v66, v67
	v_max3_f32 v144, v144, v68, v69
	v_max3_f32 v144, v144, v70, v71
	v_max3_f32 v144, v144, v72, v73
	v_max3_f32 v144, v144, v74, v75
	v_max3_f32 v144, v144, v76, v77
	s_waitcnt lgkmcnt(2)
	v_mfma_f32_32x32x16_bf16 v[16:31], v[226:229], v[246:249], v[16:31]
	v_max3_f32 v144, v144, v78, v79
	v_mov_b32_e32 v145, v144
	s_nop 1
	v_permlane32_swap_b32_e32 v144, v145
	v_max_f32_e32 v145, v145, v145
	v_max_f32_e32 v144, v144, v144
	v_max_f32_e32 v144, v144, v145
	v_sub_f32_e32 v145, v144, v222
	s_mov_b32 s8, 0x42b504f3
	v_cmp_ge_f32_e32 vcc, s8, v145
	v_max_f32_e32 v145, v222, v222
	v_max_f32_e32 v144, v145, v144
	s_waitcnt lgkmcnt(0)
	v_mfma_f32_32x32x16_bf16 v[16:31], v[230:233], v[250:253], v[16:31]
	v_sub_f32_e32 v145, v222, v144
	v_mul_f32_e32 v145, 0x3e0293ee, v145
	v_exp_f32_e32 v145, v145
	s_cmp_eq_u64 vcc, exec
	s_cselect_b64 s[8:9], -1, 0

.LBB0_618:
	s_cmp_eq_u32 s100, 1
	s_cbranch_scc1 .Lna_pvdA
	ds_read_b64_tr_b16 v[242:243], v167 offset:0
	ds_read_b64_tr_b16 v[244:245], v167 offset:0x800
	ds_read_b64_tr_b16 v[246:247], v167 offset:0x1000
	ds_read_b64_tr_b16 v[248:249], v167 offset:0x1800
	ds_read_b64_tr_b16 v[250:251], v167 offset:0x2000
	ds_read_b64_tr_b16 v[252:253], v167 offset:0x2800
	ds_read_b64_tr_b16 v[218:219], v167 offset:0x3000
	ds_read_b64_tr_b16 v[220:221], v167 offset:0x3800
	s_nop 0
	s_waitcnt lgkmcnt(6)
	v_mfma_f32_32x32x16_bf16 v[0:15], v[144:147], v[242:245], v[0:15]
	s_waitcnt lgkmcnt(4)
	v_mfma_f32_32x32x16_bf16 v[0:15], v[226:229], v[246:249], v[0:15]
	s_waitcnt lgkmcnt(2)
	v_mfma_f32_32x32x16_bf16 v[0:15], v[230:233], v[250:253], v[0:15]
	s_waitcnt lgkmcnt(0)
	v_mfma_f32_32x32x16_bf16 v[0:15], v[234:237], v[218:221], v[0:15]
	ds_read_b64_tr_b16 v[218:219], v167 offset:0x200
	ds_read_b64_tr_b16 v[220:221], v167 offset:0xa00
	ds_read_b64_tr_b16 v[242:243], v167 offset:0x1200
	ds_read_b64_tr_b16 v[244:245], v167 offset:0x1a00
	ds_read_b64_tr_b16 v[246:247], v167 offset:0x2200
	ds_read_b64_tr_b16 v[248:249], v167 offset:0x2a00
	ds_read_b64_tr_b16 v[250:251], v167 offset:0x3200
	ds_read_b64_tr_b16 v[252:253], v167 offset:0x3a00
	s_nop 0
	s_waitcnt lgkmcnt(6)
	v_mfma_f32_32x32x16_bf16 v[48:63], v[144:147], v[218:221], v[48:63]
	ds_read_b64_tr_b16 v[218:219], v167 offset:0x400
	ds_read_b64_tr_b16 v[220:221], v167 offset:0xc00
	s_waitcnt lgkmcnt(6)
	v_mfma_f32_32x32x16_bf16 v[48:63], v[226:229], v[242:245], v[48:63]
	ds_read_b64_tr_b16 v[242:243], v167 offset:0x1400
	ds_read_b64_tr_b16 v[244:245], v167 offset:0x1c00
	s_waitcnt lgkmcnt(6)
	v_mfma_f32_32x32x16_bf16 v[48:63], v[230:233], v[246:249], v[48:63]
	ds_read_b64_tr_b16 v[246:247], v167 offset:0x2400
	ds_read_b64_tr_b16 v[248:249], v167 offset:0x2c00
	s_waitcnt lgkmcnt(6)
	v_mfma_f32_32x32x16_bf16 v[48:63], v[234:237], v[250:253], v[48:63]
	ds_read_b64_tr_b16 v[250:251], v167 offset:0x3400
	ds_read_b64_tr_b16 v[252:253], v167 offset:0x3c00
	s_waitcnt lgkmcnt(6)
	v_mfma_f32_32x32x16_bf16 v[32:47], v[144:147], v[218:221], v[32:47]
	ds_read_b64_tr_b16 v[218:219], v167 offset:0x600
	ds_read_b64_tr_b16 v[220:221], v167 offset:0xe00
	s_waitcnt lgkmcnt(6)
	v_mfma_f32_32x32x16_bf16 v[32:47], v[226:229], v[242:245], v[32:47]
	ds_read_b64_tr_b16 v[242:243], v167 offset:0x1600
	ds_read_b64_tr_b16 v[244:245], v167 offset:0x1e00
	s_waitcnt lgkmcnt(6)
	v_mfma_f32_32x32x16_bf16 v[32:47], v[230:233], v[246:249], v[32:47]
	ds_read_b64_tr_b16 v[246:247], v167 offset:0x2600
	ds_read_b64_tr_b16 v[248:249], v167 offset:0x2e00
	s_waitcnt lgkmcnt(6)
	v_mfma_f32_32x32x16_bf16 v[32:47], v[234:237], v[250:253], v[32:47]
	ds_read_b64_tr_b16 v[250:251], v167 offset:0x3600
	ds_read_b64_tr_b16 v[252:253], v167 offset:0x3e00
	s_waitcnt lgkmcnt(6)
	v_mfma_f32_32x32x16_bf16 v[16:31], v[144:147], v[218:221], v[16:31]
	v_max_f32_e32 v144, v81, v81
	v_max_f32_e32 v145, v80, v80
	v_max_f32_e32 v144, v145, v144
	v_max3_f32 v144, v144, v82, v83
	v_max3_f32 v144, v144, v84, v85
	v_max3_f32 v144, v144, v86, v87
	v_max3_f32 v144, v144, v88, v89
	v_max3_f32 v144, v144, v90, v91
	v_max3_f32 v144, v144, v92, v93
	s_waitcnt lgkmcnt(4)
	v_mfma_f32_32x32x16_bf16 v[16:31], v[226:229], v[242:245], v[16:31]
	v_max3_f32 v144, v144, v94, v95
	v_max3_f32 v144, v144, v64, v65
	v_max3_f32 v144, v144, v66, v67
	v_max3_f32 v144, v144, v68, v69
	v_max3_f32 v144, v144, v70, v71
	v_max3_f32 v144, v144, v72, v73
	v_max3_f32 v144, v144, v74, v75
	v_max3_f32 v144, v144, v76, v77
	s_waitcnt lgkmcnt(2)
	v_mfma_f32_32x32x16_bf16 v[16:31], v[230:233], v[246:249], v[16:31]
	v_max3_f32 v144, v144, v78, v79
	v_mov_b32_e32 v145, v144
	s_nop 1
	v_permlane32_swap_b32_e32 v144, v145
	v_max_f32_e32 v145, v145, v145
	v_max_f32_e32 v144, v144, v144
	v_max_f32_e32 v144, v144, v145
	v_sub_f32_e32 v145, v144, v222
	s_mov_b32 s8, 0x42b504f3
	v_cmp_ge_f32_e32 vcc, s8, v145
	v_max_f32_e32 v145, v222, v222
	v_max_f32_e32 v145, v145, v144
	s_waitcnt lgkmcnt(0)
	v_mfma_f32_32x32x16_bf16 v[16:31], v[234:237], v[250:253], v[16:31]
	v_sub_f32_e32 v144, v222, v145
	v_mul_f32_e32 v144, 0x3e0293ee, v144
	v_exp_f32_e32 v144, v144
	s_cmp_eq_u64 vcc, exec
	s_cselect_b64 s[8:9], -1, 0

.LBB0_644:
	s_add_i32 s2, s27, 3
	s_cmp_lt_i32 s2, s20
	s_cselect_b64 s[8:9], -1, 0
	s_cmp_eq_u32 s101, 1
	s_cbranch_scc1 .Lwin_pvdB
	ds_read_b64_tr_b16 v[204:205], v160 offset:0
	ds_read_b64_tr_b16 v[206:207], v160 offset:0x800
	ds_read_b64_tr_b16 v[208:209], v160 offset:0x1000
	ds_read_b64_tr_b16 v[210:211], v160 offset:0x1800
	ds_read_b64_tr_b16 v[212:213], v160 offset:0x2000
	ds_read_b64_tr_b16 v[214:215], v160 offset:0x2800
	ds_read_b64_tr_b16 v[218:219], v160 offset:0x3000
	ds_read_b64_tr_b16 v[220:221], v160 offset:0x3800
	s_nop 0
	s_waitcnt lgkmcnt(6)
	v_mfma_f32_32x32x16_bf16 v[48:63], v[144:147], v[204:207], v[48:63]
	ds_read_b64_tr_b16 v[204:205], v160 offset:0x200
	ds_read_b64_tr_b16 v[206:207], v160 offset:0xa00
	s_waitcnt lgkmcnt(6)
	v_mfma_f32_32x32x16_bf16 v[48:63], v[186:189], v[208:211], v[48:63]
	ds_read_b64_tr_b16 v[208:209], v160 offset:0x1200
	ds_read_b64_tr_b16 v[210:211], v160 offset:0x1a00
	s_waitcnt lgkmcnt(6)
	v_mfma_f32_32x32x16_bf16 v[48:63], v[182:185], v[212:215], v[48:63]
	ds_read_b64_tr_b16 v[212:213], v160 offset:0x2200
	ds_read_b64_tr_b16 v[214:215], v160 offset:0x2a00
	s_waitcnt lgkmcnt(6)
	v_mfma_f32_32x32x16_bf16 v[48:63], v[200:203], v[218:221], v[48:63]
	ds_read_b64_tr_b16 v[218:219], v160 offset:0x3200
	ds_read_b64_tr_b16 v[220:221], v160 offset:0x3a00
	s_waitcnt lgkmcnt(6)
	v_mfma_f32_32x32x16_bf16 v[32:47], v[144:147], v[204:207], v[32:47]
	ds_read_b64_tr_b16 v[204:205], v160 offset:0x400
	ds_read_b64_tr_b16 v[206:207], v160 offset:0xc00
	s_waitcnt lgkmcnt(6)
	v_mfma_f32_32x32x16_bf16 v[32:47], v[186:189], v[208:211], v[32:47]
	ds_read_b64_tr_b16 v[208:209], v160 offset:0x1400
	ds_read_b64_tr_b16 v[210:211], v160 offset:0x1c00
	s_waitcnt lgkmcnt(6)
	v_mfma_f32_32x32x16_bf16 v[32:47], v[182:185], v[212:215], v[32:47]
	ds_read_b64_tr_b16 v[212:213], v160 offset:0x2400
	ds_read_b64_tr_b16 v[214:215], v160 offset:0x2c00
	s_waitcnt lgkmcnt(6)
	v_mfma_f32_32x32x16_bf16 v[32:47], v[200:203], v[218:221], v[32:47]
	ds_read_b64_tr_b16 v[218:219], v160 offset:0x3400
	ds_read_b64_tr_b16 v[220:221], v160 offset:0x3c00
	s_waitcnt lgkmcnt(6)
	v_mfma_f32_32x32x16_bf16 v[16:31], v[144:147], v[204:207], v[16:31]
	ds_read_b64_tr_b16 v[204:205], v160 offset:0x600
	ds_read_b64_tr_b16 v[206:207], v160 offset:0xe00
	s_waitcnt lgkmcnt(6)
	v_mfma_f32_32x32x16_bf16 v[16:31], v[186:189], v[208:211], v[16:31]
	ds_read_b64_tr_b16 v[208:209], v160 offset:0x1600
	ds_read_b64_tr_b16 v[210:211], v160 offset:0x1e00
	s_waitcnt lgkmcnt(6)
	v_mfma_f32_32x32x16_bf16 v[16:31], v[182:185], v[212:215], v[16:31]
	ds_read_b64_tr_b16 v[212:213], v160 offset:0x2600
	ds_read_b64_tr_b16 v[214:215], v160 offset:0x2e00
	s_waitcnt lgkmcnt(6)
	v_mfma_f32_32x32x16_bf16 v[16:31], v[200:203], v[218:221], v[16:31]
	ds_read_b64_tr_b16 v[218:219], v160 offset:0x3600
	ds_read_b64_tr_b16 v[220:221], v160 offset:0x3e00
	s_waitcnt lgkmcnt(6)
	v_mfma_f32_32x32x16_bf16 v[0:15], v[144:147], v[204:207], v[0:15]
	v_max_f32_e32 v144, v81, v81
	v_max_f32_e32 v145, v80, v80
	v_max_f32_e32 v144, v145, v144
	v_max3_f32 v144, v144, v82, v83
	v_max3_f32 v144, v144, v84, v85
	v_max3_f32 v144, v144, v86, v87
	v_max3_f32 v144, v144, v88, v89
	v_max3_f32 v144, v144, v90, v91
	v_max3_f32 v144, v144, v92, v93
	s_waitcnt lgkmcnt(4)
	v_mfma_f32_32x32x16_bf16 v[0:15], v[186:189], v[208:211], v[0:15]
	v_max3_f32 v144, v144, v94, v95
	v_max3_f32 v144, v144, v64, v65
	v_max3_f32 v144, v144, v66, v67
	v_max3_f32 v144, v144, v68, v69
	v_max3_f32 v144, v144, v70, v71
	v_max3_f32 v144, v144, v72, v73
	v_max3_f32 v144, v144, v74, v75
	v_max3_f32 v144, v144, v76, v77
	s_waitcnt lgkmcnt(2)
	v_mfma_f32_32x32x16_bf16 v[0:15], v[182:185], v[212:215], v[0:15]
	v_max3_f32 v144, v144, v78, v79
	v_mov_b32_e32 v145, v144
	s_nop 1
	v_permlane32_swap_b32_e32 v144, v145
	v_max_f32_e32 v145, v145, v145
	v_max_f32_e32 v144, v144, v144
	v_max_f32_e32 v144, v144, v145
	v_sub_f32_e32 v145, v144, v174
	s_mov_b32 s2, 0x42b504f3
	v_cmp_ge_f32_e32 vcc, s2, v145
	v_max_f32_e32 v145, v174, v174
	v_max_f32_e32 v144, v145, v144
	s_waitcnt lgkmcnt(0)
	v_mfma_f32_32x32x16_bf16 v[0:15], v[200:203], v[218:221], v[0:15]
	v_sub_f32_e32 v145, v174, v144
	v_mul_f32_e32 v145, 0x3e0293ee, v145
	v_exp_f32_e32 v145, v145
	s_cmp_eq_u64 vcc, exec
	s_cselect_b64 s[2:3], -1, 0

.LBB0_652:
	s_cmp_eq_u32 s100, 1
	s_cbranch_scc1 .Lwin_pvdA
	ds_read_b64_tr_b16 v[210:211], v177 offset:0
	ds_read_b64_tr_b16 v[212:213], v177 offset:0x800
	ds_read_b64_tr_b16 v[218:219], v177 offset:0x1000
	ds_read_b64_tr_b16 v[220:221], v177 offset:0x1800
	ds_read_b64_tr_b16 v[222:223], v177 offset:0x2000
	ds_read_b64_tr_b16 v[224:225], v177 offset:0x2800
	ds_read_b64_tr_b16 v[226:227], v177 offset:0x3000
	ds_read_b64_tr_b16 v[228:229], v177 offset:0x3800
	s_nop 0
	s_waitcnt lgkmcnt(6)
	v_mfma_f32_32x32x16_bf16 v[48:63], v[144:147], v[210:213], v[48:63]
	ds_read_b64_tr_b16 v[210:211], v177 offset:0x200
	ds_read_b64_tr_b16 v[212:213], v177 offset:0xa00
	s_waitcnt lgkmcnt(6)
	v_mfma_f32_32x32x16_bf16 v[48:63], v[182:185], v[218:221], v[48:63]
	ds_read_b64_tr_b16 v[218:219], v177 offset:0x1200
	ds_read_b64_tr_b16 v[220:221], v177 offset:0x1a00
	s_waitcnt lgkmcnt(6)
	v_mfma_f32_32x32x16_bf16 v[48:63], v[186:189], v[222:225], v[48:63]
	ds_read_b64_tr_b16 v[222:223], v177 offset:0x2200
	ds_read_b64_tr_b16 v[224:225], v177 offset:0x2a00
	s_waitcnt lgkmcnt(6)
	v_mfma_f32_32x32x16_bf16 v[48:63], v[206:209], v[226:229], v[48:63]
	ds_read_b64_tr_b16 v[226:227], v177 offset:0x3200
	ds_read_b64_tr_b16 v[228:229], v177 offset:0x3a00
	s_waitcnt lgkmcnt(6)
	v_mfma_f32_32x32x16_bf16 v[32:47], v[144:147], v[210:213], v[32:47]
	ds_read_b64_tr_b16 v[210:211], v177 offset:0x400
	ds_read_b64_tr_b16 v[212:213], v177 offset:0xc00
	s_waitcnt lgkmcnt(6)
	v_mfma_f32_32x32x16_bf16 v[32:47], v[182:185], v[218:221], v[32:47]
	ds_read_b64_tr_b16 v[218:219], v177 offset:0x1400
	ds_read_b64_tr_b16 v[220:221], v177 offset:0x1c00
	s_waitcnt lgkmcnt(6)
	v_mfma_f32_32x32x16_bf16 v[32:47], v[186:189], v[222:225], v[32:47]
	ds_read_b64_tr_b16 v[222:223], v177 offset:0x2400
	ds_read_b64_tr_b16 v[224:225], v177 offset:0x2c00
	s_waitcnt lgkmcnt(6)
	v_mfma_f32_32x32x16_bf16 v[32:47], v[206:209], v[226:229], v[32:47]
	ds_read_b64_tr_b16 v[226:227], v177 offset:0x3400
	ds_read_b64_tr_b16 v[228:229], v177 offset:0x3c00
	s_waitcnt lgkmcnt(6)
	v_mfma_f32_32x32x16_bf16 v[16:31], v[144:147], v[210:213], v[16:31]
	ds_read_b64_tr_b16 v[210:211], v177 offset:0x600
	ds_read_b64_tr_b16 v[212:213], v177 offset:0xe00
	s_waitcnt lgkmcnt(6)
	v_mfma_f32_32x32x16_bf16 v[16:31], v[182:185], v[218:221], v[16:31]
	ds_read_b64_tr_b16 v[218:219], v177 offset:0x1600
	ds_read_b64_tr_b16 v[220:221], v177 offset:0x1e00
	s_waitcnt lgkmcnt(6)
	v_mfma_f32_32x32x16_bf16 v[16:31], v[186:189], v[222:225], v[16:31]
	ds_read_b64_tr_b16 v[222:223], v177 offset:0x2600
	ds_read_b64_tr_b16 v[224:225], v177 offset:0x2e00
	s_waitcnt lgkmcnt(6)
	v_mfma_f32_32x32x16_bf16 v[16:31], v[206:209], v[226:229], v[16:31]
	ds_read_b64_tr_b16 v[226:227], v177 offset:0x3600
	ds_read_b64_tr_b16 v[228:229], v177 offset:0x3e00
	s_waitcnt lgkmcnt(6)
	v_mfma_f32_32x32x16_bf16 v[0:15], v[144:147], v[210:213], v[0:15]
	v_max_f32_e32 v144, v81, v81
	v_max_f32_e32 v145, v80, v80
	v_max_f32_e32 v144, v145, v144
	v_max3_f32 v144, v144, v82, v83
	v_max3_f32 v144, v144, v84, v85
	v_max3_f32 v144, v144, v86, v87
	v_max3_f32 v144, v144, v88, v89
	v_max3_f32 v144, v144, v90, v91
	v_max3_f32 v144, v144, v92, v93
	s_waitcnt lgkmcnt(4)
	v_mfma_f32_32x32x16_bf16 v[0:15], v[182:185], v[218:221], v[0:15]
	v_max3_f32 v144, v144, v94, v95
	v_max3_f32 v144, v144, v64, v65
	v_max3_f32 v144, v144, v66, v67
	v_max3_f32 v144, v144, v68, v69
	v_max3_f32 v144, v144, v70, v71
	v_max3_f32 v144, v144, v72, v73
	v_max3_f32 v144, v144, v74, v75
	v_max3_f32 v144, v144, v76, v77
	s_waitcnt lgkmcnt(2)
	v_mfma_f32_32x32x16_bf16 v[0:15], v[186:189], v[222:225], v[0:15]
	v_max3_f32 v144, v144, v78, v79
	v_mov_b32_e32 v145, v144
	s_nop 1
	v_permlane32_swap_b32_e32 v144, v145
	v_max_f32_e32 v145, v145, v145
	v_max_f32_e32 v144, v144, v144
	v_max_f32_e32 v144, v144, v145
	v_sub_f32_e32 v145, v144, v174
	s_mov_b32 s2, 0x42b504f3
	v_cmp_ge_f32_e32 vcc, s2, v145
	v_max_f32_e32 v145, v174, v174
	v_max_f32_e32 v145, v145, v144
	s_waitcnt lgkmcnt(0)
	v_mfma_f32_32x32x16_bf16 v[0:15], v[206:209], v[226:229], v[0:15]
	v_sub_f32_e32 v144, v174, v145
	v_mul_f32_e32 v144, 0x3e0293ee, v144
	v_exp_f32_e32 v144, v144
	s_cmp_eq_u64 vcc, exec
	s_cselect_b64 s[2:3], -1, 0
